# attention loop: K/V LDS-DMA pieces use scalar base + 32-bit lane offset (no per-lane 64-bit address adds); on v7
# speedup vs baseline: 1.0024x; 1.0020x over previous
; #define ATT_DMAK(tile, slot) do { _Pragma("unroll") for (int i = 0; i < 4; ++i) { const int pc = (wv + 8 * i) < 25 ? (wv + 8 * i) : 24; \
;         __builtin_amdgcn_global_load_lds((const unsigned*)((const char*)Kbh + (size_t)(tile) * (64 * 384) + doffK[i]), (LAS unsigned*)(lds + (slot) * KT_BYTES + pc * 1024), 16, 0, 0); } } while (0)
; #define ATT_DMAV(tile, slot) do { _Pragma("unroll") for (int i = 0; i < 3; ++i) { const int pc = (wv + 8 * i) < 18 ? (wv + 8 * i) : 17; \
;         __builtin_amdgcn_global_load_lds((const unsigned*)((const char*)Vbh + (size_t)(tile) * 128 + doffV[i]), (LAS unsigned*)(lds + VRING + (slot) * VT_BYTES + pc * 1024), 16, 0, 0); } } while (0)
; __device__ __forceinline__ void attn_unit(const bf16_t* Qrows  , const bf16_t* Kbh, const bf16_t* Vbh, int nkeys, bf16_t* Orows, LAS unsigned char* lds) {
;     ...
;     bf16x8 qf[12];
;     { const bf16_t* qr = Qrows + (size_t)(qg * 32 + l32) * 768 + hi * 8;
; #pragma unroll
;       for (int ks = 0; ks < 12; ++ks) qf[ks] = *(const bf16x8*)(qr + ks * 16); }
;     f32x16 o[4];
; #pragma unroll
;     for (int db = 0; db < 4; ++db)
; #pragma unroll
;         for (int r = 0; r < 16; ++r) o[db][r] = 0.f;
;     float mrow = -1e30f, lsum = 0.f;
;     const int nt = nkeys / 64;
;     const int wv = __builtin_amdgcn_readfirstlane(wave);
;     unsigned doffK[4], doffV[3];
; #pragma unroll
;     for (int i = 0; i < 4; ++i) { const int pc = (wv + 8 * i) < 25 ? (wv + 8 * i) : 24; const int X = pc * 1024 + lane * 16, row = X / KPITCH, col = X % KPITCH; doffK[i] = (unsigned)(row * 384 + (col < 384 ? col : 0)); }
; #pragma unroll
;     for (int i = 0; i < 3; ++i) { const int pc = (wv + 8 * i) < 18 ? (wv + 8 * i) : 17; const int Y = pc * 1024 + lane * 16, row = Y / VPITCH, col = Y % VPITCH; doffV[i] = (unsigned)(row * (NKEY * 2) + (col < 128 ? col : 0)); }
;     ...
;     ATT_DMAK(0, 0); ATT_DMAV(0, 0); ATT_DMAK(1, 1); ATT_DMAV(1, 1); if (nt > 2) ATT_DMAK(2, 2);
.LBB0_1234:
	s_lshl_b32 s1, s61, s1
	s_and_b32 s0, s1, s0
	s_or_b32 s54, s14, s0
	s_and_b32 s62, s13, 3
	s_ashr_i32 s55, s54, 31
	s_mul_i32 s1, s54, 0x600
	s_mul_hi_i32 s0, s54, 0x600
	s_add_u32 s1, s31, s1
	s_addc_u32 s0, s56, s0
	s_mul_i32 s13, s62, 0x180
	s_add_u32 s16, s1, s13
	s_addc_u32 s17, s0, 0
	s_lshl_b32 s0, s12, 2
	v_mov_b32_e32 v176, v0
	s_or_b32 s14, s62, s0
	s_mul_i32 s15, s14, 0xd8000
	v_ashrrev_i32_e32 v4, 6, v176
	v_and_b32_e32 v24, 31, v176
	v_and_b32_e32 v178, 3, v4
	s_mul_hi_i32 s13, s14, 0xd8000
	s_add_u32 s0, s57, s15
	v_lshl_or_b32 v175, v178, 5, v24
	v_mov_b64_e32 v[2:3], s[16:17]
	s_movk_i32 s16, 0x600
	s_addc_u32 s1, s58, s13
	s_mul_hi_i32 s12, s14, 0x90000
	s_mul_i32 s14, s14, 0x90000
	v_bfe_u32 v174, v176, 5, 1
	v_mad_u64_u32 v[2:3], s[16:17], v175, s16, v[2:3]
	s_add_u32 s24, s59, s14
	v_lshlrev_b32_e32 v206, 4, v174
	v_readfirstlane_b32 s16, v4
	s_addc_u32 s25, s60, s12
	v_and_b32_e32 v177, 63, v176
	v_lshl_add_u64 v[2:3], v[2:3], 0, v[206:207]
	s_min_i32 s17, s16, 24
	global_load_dwordx4 v[142:145], v[2:3], off
	global_load_dwordx4 v[138:141], v[2:3], off offset:32
	global_load_dwordx4 v[134:137], v[2:3], off offset:64
	global_load_dwordx4 v[130:133], v[2:3], off offset:96
	global_load_dwordx4 v[126:129], v[2:3], off offset:128
	global_load_dwordx4 v[122:125], v[2:3], off offset:160
	global_load_dwordx4 v[118:121], v[2:3], off offset:192
	global_load_dwordx4 v[114:117], v[2:3], off offset:224
	global_load_dwordx4 v[110:113], v[2:3], off offset:256
	global_load_dwordx4 v[106:109], v[2:3], off offset:288
	global_load_dwordx4 v[102:105], v[2:3], off offset:320
	global_load_dwordx4 v[98:101], v[2:3], off offset:352
	v_lshlrev_b32_e32 v3, 4, v177
	s_lshl_b32 s65, s17, 10
	v_or_b32_e32 v2, s65, v3
	s_mov_b32 s22, 0x51eb851f
	v_mul_hi_i32 v4, v2, s22
	v_lshrrev_b32_e32 v5, 31, v4
	v_ashrrev_i32_e32 v4, 7, v4
	v_add_u32_e32 v4, v4, v5
	v_mul_i32_i24_e32 v5, 0x190, v4
	v_sub_u32_e32 v2, v2, v5
	s_movk_i32 s21, 0x180
	s_add_i32 s18, s16, 8
	v_cmp_gt_i32_e32 vcc, s21, v2
	s_min_i32 s17, s18, 24
	s_lshl_b32 s66, s17, 10
	v_cndmask_b32_e32 v2, 0, v2, vcc
	v_mad_i32_i24 v2, v4, s21, v2
	v_or_b32_e32 v4, s66, v3
	v_mul_hi_i32 v5, v4, s22
	v_lshrrev_b32_e32 v6, 31, v5
	v_ashrrev_i32_e32 v5, 7, v5
	v_add_u32_e32 v5, v5, v6
	v_mul_i32_i24_e32 v6, 0x190, v5
	v_sub_u32_e32 v4, v4, v6
	s_add_i32 s19, s16, 16
	v_cmp_gt_i32_e32 vcc, s21, v4
	s_min_i32 s17, s19, 24
	s_lshl_b32 s67, s17, 10
	v_cndmask_b32_e32 v4, 0, v4, vcc
	v_mad_i32_i24 v4, v5, s21, v4
	v_or_b32_e32 v5, s67, v3
	v_mul_hi_i32 v6, v5, s22
	v_lshrrev_b32_e32 v7, 31, v6
	v_ashrrev_i32_e32 v6, 7, v6
	v_add_u32_e32 v6, v6, v7
	v_mul_i32_i24_e32 v7, 0x190, v6
	v_sub_u32_e32 v5, v5, v7
	s_min_i32 s17, s16, 0
	v_cmp_gt_i32_e32 vcc, s21, v5
	s_lshl_b32 s68, s17, 10
	s_add_i32 s20, s68, 0x6000
	v_cndmask_b32_e32 v5, 0, v5, vcc
	v_mad_i32_i24 v6, v6, s21, v5
	v_or_b32_e32 v5, s20, v3
	v_mul_hi_i32 v7, v5, s22
	v_lshrrev_b32_e32 v8, 31, v7
	v_ashrrev_i32_e32 v7, 7, v7
	v_add_u32_e32 v7, v7, v8
	v_mul_i32_i24_e32 v8, 0x190, v7
	v_sub_u32_e32 v5, v5, v8
	v_cmp_gt_i32_e32 vcc, s21, v5
	s_min_i32 s16, s16, 17
	s_lshl_b32 s69, s16, 10
	v_cndmask_b32_e32 v5, 0, v5, vcc
	v_mad_i32_i24 v16, v7, s21, v5
	v_or_b32_e32 v5, s69, v3
	s_mov_b32 s21, 0x38e38e39
	v_mul_hi_i32 v7, v5, s21
	v_lshrrev_b32_e32 v8, 31, v7
	v_ashrrev_i32_e32 v7, 5, v7
	v_add_u32_e32 v7, v7, v8
	s_movk_i32 s23, 0x90
	v_mul_lo_u32 v8, v7, s23
	v_sub_u32_e32 v5, v5, v8
	s_movk_i32 s22, 0x80
	v_cmp_gt_i32_e32 vcc, s22, v5
	s_movk_i32 s34, 0x1200
	v_ashrrev_i32_e32 v179, 8, v176
	v_cndmask_b32_e32 v8, 0, v5, vcc
	v_mad_u64_u32 v[18:19], s[16:17], v7, s34, v[8:9]
	s_min_i32 s16, s18, 17
	s_lshl_b32 s70, s16, 10
	v_or_b32_e32 v5, s70, v3
	v_mul_hi_i32 v7, v5, s21
	v_lshrrev_b32_e32 v8, 31, v7
	v_ashrrev_i32_e32 v7, 5, v7
	v_add_u32_e32 v7, v7, v8
	v_mul_lo_u32 v8, v7, s23
	v_sub_u32_e32 v5, v5, v8
	v_cmp_gt_i32_e32 vcc, s22, v5
	s_add_i32 s18, s65, 0
	s_mov_b32 m0, s18
	v_cndmask_b32_e32 v8, 0, v5, vcc
	v_mad_u64_u32 v[20:21], s[16:17], v7, s34, v[8:9]
	s_min_i32 s16, s19, 17
	s_lshl_b32 s71, s16, 10
	v_or_b32_e32 v3, s71, v3
	v_mul_hi_i32 v5, v3, s21
	v_lshrrev_b32_e32 v7, 31, v5
	v_ashrrev_i32_e32 v5, 5, v5
	v_add_u32_e32 v5, v5, v7
	v_mul_lo_u32 v7, v5, s23
	s_add_i32 s19, s66, 0
	v_sub_u32_e32 v3, v3, v7
	global_load_lds_dwordx4 v2, s[0:1]
	s_mov_b32 m0, s19
	s_add_i32 s21, s67, 0
	v_cmp_gt_i32_e32 vcc, s22, v3
	global_load_lds_dwordx4 v4, s[0:1]
	s_mov_b32 m0, s21
	s_add_i32 s22, s68, 0
	global_load_lds_dwordx4 v6, s[0:1]
	s_add_i32 m0, s22, 0x6000
	v_readlane_b32 s23, v255, 50
	global_load_lds_dwordx4 v16, s[0:1]
	s_add_i32 m0, s23, s69
	v_cndmask_b32_e32 v8, 0, v3, vcc
	global_load_lds_dwordx4 v18, s[24:25]
	s_add_i32 m0, s23, s70
	v_mad_u64_u32 v[22:23], s[16:17], v5, s34, v[8:9]
	global_load_lds_dwordx4 v20, s[24:25]
	s_add_i32 m0, s23, s71
	s_add_u32 s16, s0, 0x6000
	global_load_lds_dwordx4 v22, s[24:25]
	s_addc_u32 s17, s1, 0
	s_add_i32 m0, s18, 0x6400
	v_mov_b32_e32 v19, v207
	global_load_lds_dwordx4 v2, s[16:17]
	s_add_i32 m0, s19, 0x6400
	v_lshl_add_u64 v[8:9], s[24:25], 0, v[18:19]
	global_load_lds_dwordx4 v4, s[16:17]
	s_add_i32 m0, s21, 0x6400
	v_mov_b32_e32 v21, v207
	global_load_lds_dwordx4 v6, s[16:17]
	s_add_i32 m0, s22, 0xc400
	v_lshl_add_u64 v[10:11], s[24:25], 0, v[20:21]
	global_load_lds_dwordx4 v16, s[16:17]
	v_readlane_b32 s16, v255, 51
	v_lshl_add_u64 v[8:9], v[8:9], 0, s[8:9]
	s_add_i32 m0, s16, s69
	v_mov_b32_e32 v23, v207
	global_load_lds_dwordx4 v[8:9], off
	v_lshl_add_u64 v[8:9], v[10:11], 0, s[8:9]
	s_add_i32 m0, s16, s70
	v_lshl_add_u64 v[12:13], s[24:25], 0, v[22:23]
	global_load_lds_dwordx4 v[8:9], off
	s_add_i32 m0, s16, s71
	v_lshl_add_u64 v[8:9], v[12:13], 0, s[8:9]
	s_add_u32 s0, s0, 0xc000
	global_load_lds_dwordx4 v[8:9], off
	s_addc_u32 s1, s1, 0
	s_add_i32 m0, s18, 0xc800
	s_add_i32 s16, s20, 0
	global_load_lds_dwordx4 v2, s[0:1]
	s_add_i32 m0, s19, 0xc800
	v_lshl_or_b32 v3, v179, 5, v24
	global_load_lds_dwordx4 v4, s[0:1]
	s_add_i32 m0, s21, 0xc800
	s_mov_b32 s36, 0
	global_load_lds_dwordx4 v6, s[0:1]
	s_add_i32 m0, s16, 0xc800
	v_mov_b32_e32 v5, v207
	global_load_lds_dwordx4 v16, s[0:1]
	s_movk_i32 s0, 0x190
	v_mul_lo_u32 v184, v3, s0
	s_waitcnt vmcnt(0)
	s_barrier
; #define LAS __attribute__((address_space(3)))
; __device__ __forceinline__ void attn_unit(const bf16_t* Qrows  , const bf16_t* Kbh, const bf16_t* Vbh, int nkeys, bf16_t* Orows, LAS unsigned char* lds) {
;     ...
;     f32x16 sA, sB;
;     { const LAS unsigned char* kp = lds + (kh * 32 + l32) * KPITCH + hi * 16;
; #pragma unroll
;       for (int r = 0; r < 16; ++r) sA[r] = 0.f;
; #pragma unroll
;       for (int i = 0; i < 12; ++i) { const bf16x8 kf = *(const LAS bf16x8*)(kp + i * 32); sA = __builtin_amdgcn_mfma_f32_32x32x16_bf16(kf, qf[i], sA, 0, 0, 0); } }
	v_add3_u32 v185, 0, v184, v206
	ds_read_b128 v[8:11], v185
	ds_read_b128 v[12:15], v185 offset:32
	s_waitcnt vmcnt(0) lgkmcnt(0)
	v_mfma_f32_32x32x16_bf16 v[66:81], v[8:11], v[142:145], 0
	s_add_u32 s0, s84, s15
	v_mov_b32_e32 v3, v207
	v_mov_b32_e32 v7, v207
	v_mov_b32_e32 v17, v207
	s_mov_b32 s50, s36
	s_mov_b32 s51, s36
	s_addc_u32 s1, s85, s13
	v_mfma_f32_32x32x16_bf16 v[66:81], v[12:15], v[138:141], v[66:81]
	ds_read_b128 v[8:11], v185 offset:64
	ds_read_b128 v[12:15], v185 offset:96
	s_mov_b32 s37, s36
	s_mov_b32 s38, s36
	s_mov_b32 s39, s36
	s_mov_b32 s40, s36
	s_mov_b32 s41, s36
	s_mov_b32 s42, s36
	s_waitcnt lgkmcnt(1)
	v_mfma_f32_32x32x16_bf16 v[66:81], v[8:11], v[134:137], v[66:81]
	s_mov_b32 s43, s36
	s_mov_b32 s44, s36
	s_mov_b32 s45, s36
	s_mov_b32 s46, s36
	s_mov_b32 s47, s36
	s_mov_b32 s48, s36
	s_mov_b32 s49, s36
	s_waitcnt lgkmcnt(0)
	v_mfma_f32_32x32x16_bf16 v[66:81], v[12:15], v[130:133], v[66:81]
	ds_read_b128 v[8:11], v185 offset:128
	ds_read_b128 v[12:15], v185 offset:160
	v_mov_b64_e32 v[64:65], s[50:51]
	v_lshlrev_b32_e32 v181, 6, v179
	v_lshl_add_u64 v[150:151], s[0:1], 0, v[2:3]
	v_lshl_add_u64 v[152:153], s[0:1], 0, v[4:5]
	v_lshl_add_u64 v[154:155], s[0:1], 0, v[6:7]
	v_lshl_add_u64 v[156:157], s[0:1], 0, v[16:17]
	s_mov_b64 s[80:81], s[0:1]
	v_mov_b32_e32 v208, v2
	v_mov_b32_e32 v209, v4
	v_mov_b32_e32 v210, v6
	v_mov_b32_e32 v211, v16
	s_waitcnt lgkmcnt(1)
	v_mfma_f32_32x32x16_bf16 v[66:81], v[8:11], v[126:129], v[66:81]
	s_add_u32 s0, s84, s14
	v_mov_b64_e32 v[50:51], s[36:37]
	v_mul_u32_u24_e32 v182, 0x90, v24
	s_addc_u32 s1, s85, s12
	v_mov_b64_e32 v[62:63], s[48:49]
	v_mov_b64_e32 v[60:61], s[46:47]
	v_mov_b64_e32 v[58:59], s[44:45]
	s_waitcnt lgkmcnt(0)
	v_mfma_f32_32x32x16_bf16 v[66:81], v[12:15], v[122:125], v[66:81]
	ds_read_b128 v[8:11], v185 offset:192
	ds_read_b128 v[12:15], v185 offset:224
	v_mov_b64_e32 v[56:57], s[42:43]
	v_mov_b64_e32 v[54:55], s[40:41]
	v_mov_b64_e32 v[52:53], s[38:39]
	v_lshl_add_u64 v[158:159], s[0:1], 0, v[18:19]
	v_lshl_add_u64 v[160:161], s[0:1], 0, v[20:21]
	v_lshl_add_u64 v[162:163], s[0:1], 0, v[22:23]
	s_mov_b64 s[82:83], s[0:1]
	v_mov_b32_e32 v212, v18
	v_mov_b32_e32 v213, v20
	v_mov_b32_e32 v214, v22
	s_waitcnt lgkmcnt(1)
	v_mfma_f32_32x32x16_bf16 v[66:81], v[8:11], v[118:121], v[66:81]
	ds_read_b128 v[8:11], v185 offset:256
	v_mov_b64_e32 v[34:35], v[50:51]
	v_mov_b64_e32 v[18:19], v[50:51]
	s_mov_b32 s14, 1
	v_mov_b32_e32 v186, 0
	v_mov_b32_e32 v183, 0xf149f2ca
	v_mov_b64_e32 v[36:37], v[52:53]
	s_waitcnt lgkmcnt(1)
	v_mfma_f32_32x32x16_bf16 v[66:81], v[12:15], v[114:117], v[66:81]
	ds_read_b128 v[12:15], v185 offset:288
	v_mov_b64_e32 v[38:39], v[54:55]
	v_mov_b64_e32 v[40:41], v[56:57]
	v_mov_b64_e32 v[42:43], v[58:59]
	v_mov_b64_e32 v[44:45], v[60:61]
	v_mov_b64_e32 v[46:47], v[62:63]
	v_mov_b64_e32 v[48:49], v[64:65]
	s_waitcnt lgkmcnt(1)
	v_mfma_f32_32x32x16_bf16 v[66:81], v[8:11], v[110:113], v[66:81]
	ds_read_b128 v[8:11], v185 offset:320
	v_mov_b64_e32 v[20:21], v[52:53]
	v_mov_b64_e32 v[22:23], v[54:55]
	v_mov_b64_e32 v[24:25], v[56:57]
	v_mov_b64_e32 v[26:27], v[58:59]
	v_mov_b64_e32 v[28:29], v[60:61]
	v_mov_b64_e32 v[30:31], v[62:63]
	s_waitcnt lgkmcnt(1)
	v_mfma_f32_32x32x16_bf16 v[66:81], v[12:15], v[106:109], v[66:81]
	ds_read_b128 v[12:15], v185 offset:352
	v_mov_b64_e32 v[32:33], v[64:65]
	s_waitcnt lgkmcnt(1)
	v_mfma_f32_32x32x16_bf16 v[66:81], v[8:11], v[102:105], v[66:81]
	v_add_u32_e32 v8, s23, v181
	v_add3_u32 v187, v8, v206, v182
	s_waitcnt lgkmcnt(0)
	v_mfma_f32_32x32x16_bf16 v[66:81], v[12:15], v[98:101], v[66:81]
	v_mov_b64_e32 v[2:3], v[50:51]
	v_mov_b64_e32 v[4:5], v[52:53]
	v_mov_b64_e32 v[6:7], v[54:55]
	v_mov_b64_e32 v[8:9], v[56:57]
	v_mov_b64_e32 v[10:11], v[58:59]
	v_mov_b64_e32 v[12:13], v[60:61]
	v_mov_b64_e32 v[14:15], v[62:63]
	v_mov_b64_e32 v[16:17], v[64:65]
	s_branch .LBB0_1236
.LBB0_1235:
	s_add_i32 s15, s14, 1
	s_cmp_lg_u32 s14, 2
	s_cselect_b32 s14, s15, 0
	s_mul_i32 s15, s14, 0x6400
	v_add_u32_e32 v70, s15, v185
	ds_read_b128 v[66:69], v70
	ds_read_b128 v[166:169], v70 offset:32
	ds_read_b128 v[170:173], v70 offset:64
	ds_read_b128 v[188:191], v70 offset:96
	ds_read_b128 v[192:195], v70 offset:128
	ds_read_b128 v[196:199], v70 offset:160
	ds_read_b128 v[200:203], v70 offset:192
	ds_read_b128 v[216:219], v70 offset:224
	ds_read_b128 v[220:223], v70 offset:256
	ds_read_b128 v[224:227], v70 offset:288
	ds_read_b128 v[228:231], v70 offset:320
	ds_read_b128 v[146:149], v70 offset:352
	s_waitcnt lgkmcnt(11)
	v_mfma_f32_32x32x16_bf16 v[66:81], v[66:69], v[142:145], 0
	v_sub_f32_e32 v82, v82, v183
	v_exp_f32_e32 v82, v82
	v_sub_f32_e32 v94, v94, v183
	v_exp_f32_e32 v94, v94
	v_add_f32_e32 v165, 0, v82
	v_add_f32_e32 v165, v94, v165
	s_waitcnt lgkmcnt(10)
	v_mfma_f32_32x32x16_bf16 v[66:81], v[166:169], v[138:141], v[66:81]
	v_sub_f32_e32 v83, v83, v183
	v_exp_f32_e32 v83, v83
	v_sub_f32_e32 v95, v95, v183
	v_exp_f32_e32 v95, v95
	v_add_f32_e32 v165, v83, v165
	v_cvt_pk_bf16_f32 v82, v82, v83
	v_add_f32_e32 v165, v95, v165
	v_sub_f32_e32 v83, v84, v183
	s_waitcnt lgkmcnt(9)
	v_mfma_f32_32x32x16_bf16 v[66:81], v[170:173], v[134:137], v[66:81]
	v_exp_f32_e32 v83, v83
	v_sub_f32_e32 v96, v96, v183
	v_add_f32_e32 v84, v83, v165
	v_exp_f32_e32 v165, v96
	s_nop 0
	v_add_f32_e32 v84, v165, v84
	s_waitcnt lgkmcnt(8)
	v_mfma_f32_32x32x16_bf16 v[66:81], v[188:191], v[130:133], v[66:81]
	v_sub_f32_e32 v85, v85, v183
	v_exp_f32_e32 v85, v85
	v_sub_f32_e32 v96, v97, v183
	v_exp_f32_e32 v97, v96
	v_cvt_pk_bf16_f32 v96, v94, v95
	v_add_f32_e32 v84, v85, v84
	v_cvt_pk_bf16_f32 v83, v83, v85
	v_add_f32_e32 v84, v97, v84
	v_cvt_pk_bf16_f32 v97, v165, v97
	s_waitcnt lgkmcnt(7)
; #define LAS __attribute__((address_space(3)))
; #define ATT_DMAK(tile, slot) do { _Pragma("unroll") for (int i = 0; i < 4; ++i) { const int pc = (wv + 8 * i) < 25 ? (wv + 8 * i) : 24; \
;         __builtin_amdgcn_global_load_lds((const unsigned*)((const char*)Kbh + (size_t)(tile) * (64 * 384) + doffK[i]), (LAS unsigned*)(lds + (slot) * KT_BYTES + pc * 1024), 16, 0, 0); } } while (0)
; #define ATT_DMAV(tile, slot) do { _Pragma("unroll") for (int i = 0; i < 3; ++i) { const int pc = (wv + 8 * i) < 18 ? (wv + 8 * i) : 17; \
;         __builtin_amdgcn_global_load_lds((const unsigned*)((const char*)Vbh + (size_t)(tile) * 128 + doffV[i]), (LAS unsigned*)(lds + VRING + (slot) * VT_BYTES + pc * 1024), 16, 0, 0); } } while (0)
; #define ATT_SYNC(full) do { if (full) asm volatile("s_waitcnt vmcnt(7)" ::: "memory"); else asm volatile("s_waitcnt vmcnt(0)" ::: "memory"); \
;         __builtin_amdgcn_s_barrier(); asm volatile("" ::: "memory"); } while (0)
; __device__ __forceinline__ void attn_unit(const bf16_t* Qrows  , const bf16_t* Kbh, const bf16_t* Vbh, int nkeys, bf16_t* Orows, LAS unsigned char* lds) {
;     ...
;     ATT_DMAK(0, 0); ATT_DMAV(0, 0); ATT_DMAK(1, 1); ATT_DMAV(1, 1); if (nt > 2) ATT_DMAK(2, 2);
;     asm volatile("s_waitcnt vmcnt(0)" ::: "memory");
;     __builtin_amdgcn_s_barrier(); asm volatile("" ::: "memory");
;     f32x16 sA, sB;
;     { const LAS unsigned char* kp = lds + (kh * 32 + l32) * KPITCH + hi * 16;
; #pragma unroll
;       for (int r = 0; r < 16; ++r) sA[r] = 0.f;
; #pragma unroll
;       for (int i = 0; i < 12; ++i) { const bf16x8 kf = *(const LAS bf16x8*)(kp + i * 32); sA = __builtin_amdgcn_mfma_f32_32x32x16_bf16(kf, qf[i], sA, 0, 0, 0); } }
;     int k1 = 1, v0 = 0;
;     int j = 0;
;     for (; j + 2 < nt; j += 2) {
;         ATT_SYNC(true);
;         if (j + 3 < nt) ATT_DMAK(j + 3, v0);
;         ATT_DMAV(j + 2, v0 == 0 ? 2 : v0 - 1);
;         ATT_STEP(sA, sB, true, k1, v0);
;         k1 = k1 == 2 ? 0 : k1 + 1; v0 = v0 == 2 ? 0 : v0 + 1;
;         ATT_SYNC(j + 3 < nt);
;         if (j + 4 < nt) ATT_DMAK(j + 4, v0);
;         if (j + 3 < nt) ATT_DMAV(j + 3, v0 == 0 ? 2 : v0 - 1);
;         ATT_STEP(sB, sA, true, k1, v0);
	v_mfma_f32_32x32x16_bf16 v[66:81], v[192:195], v[126:129], v[66:81]
	v_sub_f32_e32 v85, v86, v183
	v_exp_f32_e32 v85, v85
	s_nop 0
	v_add_f32_e32 v84, v85, v84
	s_waitcnt lgkmcnt(6)
	v_mfma_f32_32x32x16_bf16 v[66:81], v[196:199], v[122:125], v[66:81]
	v_sub_f32_e32 v86, v87, v183
	v_exp_f32_e32 v86, v86
	s_nop 0
	v_add_f32_e32 v87, v86, v84
	v_cvt_pk_bf16_f32 v84, v85, v86
	s_waitcnt lgkmcnt(5)
	v_mfma_f32_32x32x16_bf16 v[66:81], v[200:203], v[118:121], v[66:81]
	v_sub_f32_e32 v85, v88, v183
	v_exp_f32_e32 v85, v85
	s_nop 0
	v_add_f32_e32 v86, v85, v87
	s_waitcnt lgkmcnt(4)
	v_mfma_f32_32x32x16_bf16 v[66:81], v[216:219], v[114:117], v[66:81]
	v_sub_f32_e32 v87, v89, v183
	v_exp_f32_e32 v87, v87
	s_nop 0
	v_add_f32_e32 v86, v87, v86
	v_cvt_pk_bf16_f32 v85, v85, v87
	v_sub_f32_e32 v87, v90, v183
	v_exp_f32_e32 v90, v87
	s_waitcnt lgkmcnt(3)
	v_mfma_f32_32x32x16_bf16 v[66:81], v[220:223], v[110:113], v[66:81]
	v_add_u32_e32 v165, s13, v187
	v_add_f32_e32 v94, v90, v86
	ds_read_b128 v[86:89], v165
	ds_read_b128 v[166:169], v165 offset:32
	s_waitcnt lgkmcnt(4)
	v_mfma_f32_32x32x16_bf16 v[66:81], v[224:227], v[106:109], v[66:81]
	v_sub_f32_e32 v91, v91, v183
	ds_read_b128 v[170:173], v165 offset:4608
	ds_read_b128 v[188:191], v165 offset:4640
	v_exp_f32_e32 v91, v91
	s_nop 0
	v_add_f32_e32 v95, v91, v94
	v_cvt_pk_bf16_f32 v94, v90, v91
	s_waitcnt lgkmcnt(5)
	v_mfma_f32_32x32x16_bf16 v[66:81], v[228:231], v[102:105], v[66:81]
	v_sub_f32_e32 v90, v92, v183
	ds_read_b128 v[192:195], v165 offset:9216
	ds_read_b128 v[196:199], v165 offset:9248
	v_exp_f32_e32 v90, v90
	s_nop 0
	v_add_f32_e32 v91, v90, v95
	v_sub_f32_e32 v92, v93, v183
	v_exp_f32_e32 v92, v92
	s_waitcnt lgkmcnt(6)
	v_mfma_f32_32x32x16_bf16 v[66:81], v[146:149], v[98:101], v[66:81]
	v_add_f32_e32 v186, v92, v91
	v_cvt_pk_bf16_f32 v95, v90, v92
	ds_read_b128 v[90:93], v165 offset:13824
	ds_read_b128 v[146:149], v165 offset:13856
	s_waitcnt lgkmcnt(0)
	v_mfma_f32_32x32x16_bf16 v[50:65], v[86:89], v[82:85], v[50:65]
	v_add_f32_e32 v186, v164, v186
	v_mfma_f32_32x32x16_bf16 v[34:49], v[170:173], v[82:85], v[34:49]
	v_mfma_f32_32x32x16_bf16 v[18:33], v[192:195], v[82:85], v[18:33]
	v_mfma_f32_32x32x16_bf16 v[2:17], v[90:93], v[82:85], v[2:17]
	v_mfma_f32_32x32x16_bf16 v[50:65], v[166:169], v[94:97], v[50:65]
	v_mfma_f32_32x32x16_bf16 v[34:49], v[188:191], v[94:97], v[34:49]
	v_mfma_f32_32x32x16_bf16 v[18:33], v[196:199], v[94:97], v[18:33]
	v_mfma_f32_32x32x16_bf16 v[2:17], v[146:149], v[94:97], v[2:17]
	s_add_i32 s13, s14, 1
	s_cmp_lg_u32 s14, 2
	s_cselect_b32 s14, s13, 0
	s_add_i32 s13, s12, 1
	s_cmp_lg_u32 s12, 2
	s_cselect_b32 s36, s13, 0
	s_add_u32 s80, s80, s6
	s_addc_u32 s81, s81, s7
	s_add_u32 s82, s82, s10
	s_addc_u32 s83, s83, s11
	s_add_i32 s63, s63, 2
	s_andn2_b64 vcc, exec, s[0:1]
	s_cbranch_vccz .LBB0_1250
.LBB0_1236:
	s_add_i32 s0, s63, -1
	s_cmp_lt_u32 s0, s64
	s_waitcnt vmcnt(7)
	s_barrier
	s_cselect_b64 s[24:25], -1, 0
	s_cmp_ge_u32 s0, s64
	s_cselect_b64 s[0:1], -1, 0
	s_and_b64 vcc, exec, s[0:1]
	s_cbranch_vccnz .LBB0_1238
	s_mul_i32 s12, s36, 0x6400
	s_add_i32 s12, s12, 0
	s_add_u32 s16, s80, s2
	s_addc_u32 s17, s81, s3
	s_add_u32 s16, s16, 0x30e8a000
	s_addc_u32 s17, s17, 0
	s_add_i32 m0, s12, s65
	s_nop 0
	global_load_lds_dwordx4 v208, s[16:17]
	s_add_i32 m0, s12, s66
	s_nop 0
	global_load_lds_dwordx4 v209, s[16:17]
	s_add_i32 m0, s12, s67
	s_add_i32 s12, s12, s68
	global_load_lds_dwordx4 v210, s[16:17]
	s_add_i32 m0, s12, 0x6000
	s_nop 0
	global_load_lds_dwordx4 v211, s[16:17]
.LBB0_1238:
	s_mul_i32 s12, s36, 0x4800
	s_add_i32 s13, s12, 0xffffb800
	s_cmp_lg_u32 s36, 0
	s_cselect_b32 s13, s13, 0x9000
	s_add_i32 s13, s13, 0
	s_add_i32 s13, s13, 0x12c00
	s_add_u32 s16, s82, s2
	s_addc_u32 s17, s83, s3
	s_add_u32 s16, s16, s28
	s_addc_u32 s17, s17, s29
	s_add_i32 m0, s13, s69
	s_nop 0
	global_load_lds_dwordx4 v212, s[16:17]
	s_add_i32 m0, s13, s70
	s_nop 0
	global_load_lds_dwordx4 v213, s[16:17]
	s_add_i32 m0, s13, s71
	v_and_b32_e32 v84, 64, v249
	global_load_lds_dwordx4 v214, s[16:17]
	v_max_f32_e32 v82, v67, v67
	v_max_f32_e32 v83, v66, v66
	v_max_f32_e32 v82, v83, v82
	v_max3_f32 v82, v82, v68, v69
	v_max3_f32 v82, v82, v70, v71
	v_max3_f32 v82, v82, v72, v73
	v_max3_f32 v82, v82, v74, v75
	v_xor_b32_e32 v83, 32, v249
	v_add_u32_e32 v84, 64, v84
	v_max3_f32 v82, v82, v76, v77
	v_cmp_lt_i32_e32 vcc, v83, v84
	v_max3_f32 v82, v82, v78, v79
	v_max3_f32 v82, v82, v80, v81
	v_cndmask_b32_e32 v83, v249, v83, vcc
	v_lshlrev_b32_e32 v180, 2, v83
	v_mov_b32_e32 v83, v82
	s_nop 1
	v_permlane32_swap_b32_e32 v83, v82
	s_waitcnt lgkmcnt(0)
	v_max_f32_e32 v83, v83, v83
	v_max_f32_e32 v82, v82, v83
	v_add_f32_e32 v83, 0x41000000, v183
	v_cmp_gt_f32_e32 vcc, v82, v83
	s_cbranch_vccz .LBB0_1240
	v_max_f32_e32 v82, v82, v82
	v_max_f32_e32 v83, v183, v183
	v_max_f32_e32 v83, v83, v82
	v_sub_f32_e32 v82, v183, v83
	v_exp_f32_e32 v82, v82
	v_mov_b32_e32 v183, v83
	v_pk_mul_f32 v[64:65], v[64:65], v[82:83] op_sel_hi:[1,0]
	v_pk_mul_f32 v[62:63], v[62:63], v[82:83] op_sel_hi:[1,0]
	v_pk_mul_f32 v[60:61], v[60:61], v[82:83] op_sel_hi:[1,0]
	v_pk_mul_f32 v[58:59], v[58:59], v[82:83] op_sel_hi:[1,0]
	v_pk_mul_f32 v[56:57], v[56:57], v[82:83] op_sel_hi:[1,0]
	v_pk_mul_f32 v[54:55], v[54:55], v[82:83] op_sel_hi:[1,0]
	v_pk_mul_f32 v[52:53], v[52:53], v[82:83] op_sel_hi:[1,0]
	v_pk_mul_f32 v[50:51], v[50:51], v[82:83] op_sel_hi:[1,0]
	v_pk_mul_f32 v[48:49], v[48:49], v[82:83] op_sel_hi:[1,0]
	v_pk_mul_f32 v[46:47], v[46:47], v[82:83] op_sel_hi:[1,0]
	v_pk_mul_f32 v[44:45], v[44:45], v[82:83] op_sel_hi:[1,0]
	v_pk_mul_f32 v[42:43], v[42:43], v[82:83] op_sel_hi:[1,0]
	v_pk_mul_f32 v[40:41], v[40:41], v[82:83] op_sel_hi:[1,0]
	v_pk_mul_f32 v[38:39], v[38:39], v[82:83] op_sel_hi:[1,0]
	v_pk_mul_f32 v[36:37], v[36:37], v[82:83] op_sel_hi:[1,0]
	v_pk_mul_f32 v[34:35], v[34:35], v[82:83] op_sel_hi:[1,0]
	v_pk_mul_f32 v[32:33], v[32:33], v[82:83] op_sel_hi:[1,0]
	v_pk_mul_f32 v[30:31], v[30:31], v[82:83] op_sel_hi:[1,0]
	v_pk_mul_f32 v[28:29], v[28:29], v[82:83] op_sel_hi:[1,0]
	v_pk_mul_f32 v[26:27], v[26:27], v[82:83] op_sel_hi:[1,0]
	v_pk_mul_f32 v[24:25], v[24:25], v[82:83] op_sel_hi:[1,0]
	v_pk_mul_f32 v[22:23], v[22:23], v[82:83] op_sel_hi:[1,0]
	v_pk_mul_f32 v[20:21], v[20:21], v[82:83] op_sel_hi:[1,0]
	v_pk_mul_f32 v[18:19], v[18:19], v[82:83] op_sel_hi:[1,0]
	v_pk_mul_f32 v[16:17], v[16:17], v[82:83] op_sel_hi:[1,0]
	v_pk_mul_f32 v[14:15], v[14:15], v[82:83] op_sel_hi:[1,0]
	v_pk_mul_f32 v[12:13], v[12:13], v[82:83] op_sel_hi:[1,0]
	v_pk_mul_f32 v[10:11], v[10:11], v[82:83] op_sel_hi:[1,0]
	v_pk_mul_f32 v[8:9], v[8:9], v[82:83] op_sel_hi:[1,0]
	v_pk_mul_f32 v[6:7], v[6:7], v[82:83] op_sel_hi:[1,0]
	v_pk_mul_f32 v[4:5], v[4:5], v[82:83] op_sel_hi:[1,0]
	v_pk_mul_f32 v[2:3], v[2:3], v[82:83] op_sel_hi:[1,0]
	v_mul_f32_e32 v186, v186, v82

; #define ATT_DMAK(tile, slot) do { _Pragma("unroll") for (int i = 0; i < 4; ++i) { const int pc = (wv + 8 * i) < 25 ? (wv + 8 * i) : 24; \
;         __builtin_amdgcn_global_load_lds((const unsigned*)((const char*)Kbh + (size_t)(tile) * (64 * 384) + doffK[i]), (LAS unsigned*)(lds + (slot) * KT_BYTES + pc * 1024), 16, 0, 0); } } while (0)
; #define ATT_DMAV(tile, slot) do { _Pragma("unroll") for (int i = 0; i < 3; ++i) { const int pc = (wv + 8 * i) < 18 ? (wv + 8 * i) : 17; \
;         __builtin_amdgcn_global_load_lds((const unsigned*)((const char*)Vbh + (size_t)(tile) * 128 + doffV[i]), (LAS unsigned*)(lds + VRING + (slot) * VT_BYTES + pc * 1024), 16, 0, 0); } } while (0)
; #define ATT_SYNC(full) do { if (full) asm volatile("s_waitcnt vmcnt(7)" ::: "memory"); else asm volatile("s_waitcnt vmcnt(0)" ::: "memory"); \
;         __builtin_amdgcn_s_barrier(); asm volatile("" ::: "memory"); } while (0)
; __device__ __forceinline__ void attn_unit(const bf16_t* Qrows  , const bf16_t* Kbh, const bf16_t* Vbh, int nkeys, bf16_t* Orows, LAS unsigned char* lds) {
;     ...
;         ATT_SYNC(j + 3 < nt);
;         if (j + 4 < nt) ATT_DMAK(j + 4, v0);
;         if (j + 3 < nt) ATT_DMAV(j + 3, v0 == 0 ? 2 : v0 - 1);
.LBB0_1244:
	s_add_i32 s0, s36, 1
	s_cmp_lg_u32 s36, 2
	s_cselect_b32 s12, s0, 0
	s_barrier
	s_cmp_ge_u32 s63, s64
	s_cselect_b64 s[0:1], -1, 0
	s_and_b64 vcc, exec, s[0:1]
	s_cbranch_vccnz .LBB0_1246
	s_mul_i32 s13, s12, 0x6400
	s_add_i32 s13, s13, 0
	s_add_u32 s16, s80, s2
	s_addc_u32 s17, s81, s3
	s_add_u32 s16, s16, 0x30e90000
	s_addc_u32 s17, s17, 0
	s_add_i32 m0, s13, s65
	s_nop 0
	global_load_lds_dwordx4 v208, s[16:17]
	s_add_i32 m0, s13, s66
	s_nop 0
	global_load_lds_dwordx4 v209, s[16:17]
	s_add_i32 m0, s13, s67
	s_add_i32 s13, s13, s68
	global_load_lds_dwordx4 v210, s[16:17]
	s_add_i32 m0, s13, 0x6000
	s_nop 0
	global_load_lds_dwordx4 v211, s[16:17]
.LBB0_1246:
	s_andn2_b64 vcc, exec, s[24:25]
	s_mul_i32 s13, s12, 0x4800
	s_cbranch_vccnz .LBB0_1248
	s_add_i32 s15, s13, 0xffffb800
	s_cmp_lg_u32 s12, 0
	s_cselect_b32 s15, s15, 0x9000
	s_add_i32 s15, s15, 0
	s_add_i32 s15, s15, 0x12c00
	s_add_u32 s16, s82, s2
	s_addc_u32 s17, s83, s3
	s_add_u32 s16, s16, 0x31bf8180
	s_addc_u32 s17, s17, 0
	s_add_i32 m0, s15, s69
	s_nop 0
	global_load_lds_dwordx4 v212, s[16:17]
	s_add_i32 m0, s15, s70
	s_nop 0
	global_load_lds_dwordx4 v213, s[16:17]
	s_add_i32 m0, s15, s71
	s_nop 0
	global_load_lds_dwordx4 v214, s[16:17]
